# v43 + gate_up: the next unit's first fragment reads issued inside the swiglu epilogue (peeled first iteration skips them), loop heads pinned at v43's offsets
# baseline (speedup 1.0000x reference)
;     __device__ __forceinline__ void a_ready(const Unit&) const { if (++ncall == 3 && sig != nullptr && threadIdx.x == 0) __hip_atomic_fetch_add(sig, 1u, __ATOMIC_RELAXED, __HIP_MEMORY_SCOPE_AGENT); }
;     __device__ bool next(int i, Unit& u) const { if (!base.next(i >> 1, u)) return false; if (i & 1) { u.pm += MTOK / BM; u.pn += DM / BM; } return true; }
; #define PG8_STAGE(bufoff, gbase, voff) do { _Pragma("unroll") for (int _i = 0; _i < 2; ++_i) \
;         __builtin_amdgcn_global_load_lds((const unsigned*)((const char*)(gbase) + (voff)[_i]), (PG8_LAS unsigned*)(lds + (bufoff) + ldsw + _i * 8192), 16, 0, 0); } while (0)
; #define PG8_LDA(dst, b, h) do { _Pragma("unroll") for (int m = 0; m < 4; ++m) _Pragma("unroll") for (int k = 0; k < 2; ++k) dst[m][k] = *(const PG8_LAS bf16x8*)(lds + PG8_SA(b, h) + aoff + m * 2048 + k * 1024); } while (0)
; #define PG8_LDB(dst, b, h) do { _Pragma("unroll") for (int n = 0; n < 2; ++n) _Pragma("unroll") for (int k = 0; k < 2; ++k) dst[n][k] = *(const PG8_LAS bf16x8*)(lds + PG8_SB(b, h) + boff + n * 2048 + k * 1024); } while (0)
; #define PG8_SCHED __builtin_amdgcn_sched_barrier(0)
;   __device__ __forceinline__ bool next(int i,AttnUnit&u)const{ if(i>=2||vcu>=256)return false; const int s=vcu&3; u.bh=vcu>>2; u.qb=(i==0)?7-s:s; return true; }
; template <class Epi, class Sched, bool ALIGN_EPI = false, bool SP2 = false>
; __device__ __forceinline__ void gemm_phase(PG8_LAS unsigned char* lds, const Gemm g, const Sched& S, const Epi& E) {
;     ...
;         const bool has_next = S.next(ui + 1, nxt);
;         const char* nA = has_next ? (const char*)g.A + (size_t)nxt.pm * tstep + (nxt.half == 2 ? hstep : (size_t)0) : cA; const char* nB = has_next ? (const char*)g.Bt + (size_t)nxt.pn * tstep : cB;
;         for (int t = 0; t < nt; t += 2) {
;             const bool last = (t == nt - 2);
;             const char* a1 = cA + (size_t)(t + 1) * kstep;
;             const char* a2 = last ? nA : cA + (size_t)(t + 2) * kstep; const char* b2 = last ? nB : cB + (size_t)(t + 2) * kstep;
;             const char* a3 = a2 + kstep; const char* b3 = b2 + kstep;
;             if (last && has_next) S.a_ready(nxt);
;             if constexpr (SP2) {
;             PG8_LDB(B0, 0, 0); PG8_LDB(B1, 0, 1); PG8_SCHED; PG8_LDA(At, 0, 0); PG8_STAGE(PG8_SA(1, 1), a1 + hstep, voffA);
.LBB0_1476:
	s_ashr_i32 s17, s16, 31
	s_lshl_b64 s[28:29], s[16:17], 19
	s_add_u32 s56, s30, s28
	s_addc_u32 s57, s31, s29
	s_and_b64 s[28:29], s[38:39], exec
	s_cselect_b32 s17, s57, s27
	s_cselect_b32 s62, s56, s26
	s_ashr_i32 s19, s18, 31
	s_lshl_b64 s[28:29], s[18:19], 19
	s_add_u32 s58, s34, s28
	s_addc_u32 s59, s35, s29
	s_and_b64 s[28:29], s[38:39], exec
	s_cselect_b32 s19, s59, s1
	s_cselect_b32 s63, s58, s0
	s_add_u32 s26, s26, 0x40080
	s_addc_u32 s27, s27, 0
	s_add_u32 s64, s0, 0x100
	s_addc_u32 s65, s1, 0
	s_mov_b32 s66, -2
	s_add_u32 s0, s26, 0xfffc0080
	s_addc_u32 s1, s27, -1
	s_add_i32 s67, 0, 0x10000
	s_cmp_eq_u32 s66, 12
	s_cselect_b32 s29, s17, s1
	s_cselect_b32 s28, s62, s0
	s_cselect_b32 s1, s19, s65
	s_cselect_b32 s0, s63, s64
	s_add_i32 s70, 0, 0x14000
	s_cmp_lg_u32 s32, 0
	s_cbranch_scc1 .Lpr_gu
	v_add_u32_e32 v151, s67, v147
	ds_read_b128 v[142:145], v151
	ds_read_b128 v[152:155], v151 offset:1024
	ds_read_b128 v[156:159], v151 offset:2048
	ds_read_b128 v[160:163], v151 offset:3072
	v_add_u32_e32 v151, s70, v147
	ds_read_b128 v[164:167], v151
	ds_read_b128 v[168:171], v151 offset:1024
	ds_read_b128 v[172:175], v151 offset:2048
	ds_read_b128 v[176:179], v151 offset:3072
	ds_read_b128 v[180:183], v150
	ds_read_b128 v[184:187], v150 offset:1024
	ds_read_b128 v[188:191], v150 offset:2048
	ds_read_b128 v[192:195], v150 offset:3072
	ds_read_b128 v[196:199], v150 offset:4096
	ds_read_b128 v[200:203], v150 offset:5120
	ds_read_b128 v[204:207], v150 offset:6144
	ds_read_b128 v[208:211], v150 offset:7168
.Lpr_gu:
	v_lshl_add_u64 v[212:213], s[26:27], 0, v[138:139]
	s_add_i32 m0, s15, 0xc000
	global_load_lds_dwordx4 v[212:213], off
	v_lshl_add_u64 v[212:213], s[26:27], 0, v[140:141]
	s_add_i32 m0, s15, 0xe000
	s_nop 0
	global_load_lds_dwordx4 v[212:213], off
	s_cmp_eq_u32 s32, 0
	s_cbranch_scc1 .Lpw_gu_1
	s_waitcnt vmcnt(16)
	s_branch .Lpj_gu_1

; #define PG8_LAS __attribute__((address_space(3)))
; __device__ __forceinline__ float sigm(float x) { return __builtin_amdgcn_rcpf(1.0f + __builtin_amdgcn_exp2f(-1.4426950408889634f * x)); }
; __device__ __forceinline__ u32x4 pack8(const f32x4 a, const f32x4 b) { u32x4 w; w.x = cvt_pk_bf16(a[0], a[1]); w.y = cvt_pk_bf16(a[2], a[3]); w.z = cvt_pk_bf16(b[0], b[1]); w.w = cvt_pk_bf16(b[2], b[3]); return w; }
;     __device__ __forceinline__ void operator()(const f32x4 (&acc)[2][2][4][2], const Unit& u, int wr, int wc, int fr, int fq) const {
;         const int rl0 = wr * 64 + fr + (u.half == 2 ? HALF : 0), row0 = u.pm * BM + rl0, col0 = u.pn * HALF + wc * 32 + 8 * fq; const PG8_LAS float* rsr = rsl + rl0;
; #pragma unroll
;         for (int ai = 0; ai < 2; ++ai) { if (ai == 1 && u.half != 0) break;
; #pragma unroll
;             for (int m = 0; m < 4; ++m) { const float rf = rsr[ai * HALF + m * 16]; f32x4 v0 = acc[ai][0][m][0] * rf, v1 = acc[ai][0][m][1] * rf; const f32x4 u0 = acc[ai][1][m][0] * rf, u1 = acc[ai][1][m][1] * rf;
; #pragma unroll
;                 for (int e = 0; e < 4; ++e) { v0[e] = v0[e] * sigm(v0[e]) * u0[e]; v1[e] = v1[e] * sigm(v1[e]) * u1[e]; }
;                 *(u32x4*)(H + (size_t)(row0 + ai * HALF + m * 16) * DFF + col0) = pack8(v0, v1); } }
;     }
.LBB0_1480:
	ds_read_b32 v236, v148
	ds_read_b32 v237, v148 offset:64
	ds_read_b32 v238, v148 offset:128
	ds_read_b32 v239, v148 offset:192
	ds_read_b32 v240, v148 offset:512
	ds_read_b32 v241, v148 offset:576
	ds_read_b32 v242, v148 offset:640
	ds_read_b32 v243, v148 offset:704
	v_lshl_or_b32 v252, s20, 7, v149
	v_lshl_add_u32 v253, s14, 8, v146
	v_lshlrev_b32_e32 v252, 1, v252
	v_mad_u32_u24 v252, v253, s2, v252
	v_add_u32_e32 v151, 0x10000, v147
	ds_read_b128 v[142:145], v151
	ds_read_b128 v[152:155], v151 offset:1024
	ds_read_b128 v[156:159], v151 offset:2048
	ds_read_b128 v[160:163], v151 offset:3072
	s_mov_b32 s0, 0xbfb8aa3b
	s_waitcnt lgkmcnt(4)
	v_pk_mul_f32 v[244:245], v[236:237], s[0:1] op_sel_hi:[1,0]
	v_pk_mul_f32 v[246:247], v[238:239], s[0:1] op_sel_hi:[1,0]
	v_pk_mul_f32 v[248:249], v[240:241], s[0:1] op_sel_hi:[1,0]
	v_pk_mul_f32 v[250:251], v[242:243], s[0:1] op_sel_hi:[1,0]
	v_pk_mul_f32 v[236:237], v[236:237], v[236:237]
	v_pk_mul_f32 v[238:239], v[238:239], v[238:239]
	v_pk_mul_f32 v[240:241], v[240:241], v[240:241]
	v_pk_mul_f32 v[242:243], v[242:243], v[242:243]
	v_rcp_f32_e32 v236, v236
	v_rcp_f32_e32 v237, v237
	v_rcp_f32_e32 v238, v238
	v_rcp_f32_e32 v239, v239
	v_rcp_f32_e32 v240, v240
	v_rcp_f32_e32 v241, v241
	v_rcp_f32_e32 v242, v242
	v_rcp_f32_e32 v243, v243
	v_add_u32_e32 v151, 0x14000, v147
	ds_read_b128 v[164:167], v151
	ds_read_b128 v[168:171], v151 offset:1024
	ds_read_b128 v[172:175], v151 offset:2048
	ds_read_b128 v[176:179], v151 offset:3072
	ds_read_b128 v[180:183], v150
	ds_read_b128 v[184:187], v150 offset:1024
	ds_read_b128 v[188:191], v150 offset:2048
	ds_read_b128 v[192:195], v150 offset:3072
	ds_read_b128 v[196:199], v150 offset:4096
	ds_read_b128 v[200:203], v150 offset:5120
	ds_read_b128 v[204:207], v150 offset:6144
	ds_read_b128 v[208:211], v150 offset:7168
	v_pk_mul_f32 v[228:229], v[128:129], v[244:245] op_sel:[0,0] op_sel_hi:[1,0]
	v_pk_mul_f32 v[230:231], v[130:131], v[244:245] op_sel:[0,0] op_sel_hi:[1,0]
	v_pk_mul_f32 v[232:233], v[124:125], v[244:245] op_sel:[0,0] op_sel_hi:[1,0]
	v_pk_mul_f32 v[234:235], v[126:127], v[244:245] op_sel:[0,0] op_sel_hi:[1,0]
	v_exp_f32_e32 v228, v228
	v_exp_f32_e32 v229, v229
	v_exp_f32_e32 v230, v230
	v_exp_f32_e32 v231, v231
	v_exp_f32_e32 v232, v232
	v_exp_f32_e32 v233, v233
	v_exp_f32_e32 v234, v234
	v_exp_f32_e32 v235, v235
	v_pk_fma_f32 v[228:229], v[228:229], v[236:237], v[236:237] op_sel:[0,0,0] op_sel_hi:[1,0,0]
	v_pk_fma_f32 v[230:231], v[230:231], v[236:237], v[236:237] op_sel:[0,0,0] op_sel_hi:[1,0,0]
	v_pk_fma_f32 v[232:233], v[232:233], v[236:237], v[236:237] op_sel:[0,0,0] op_sel_hi:[1,0,0]
	v_pk_fma_f32 v[234:235], v[234:235], v[236:237], v[236:237] op_sel:[0,0,0] op_sel_hi:[1,0,0]
	v_rcp_f32_e32 v228, v228
	v_rcp_f32_e32 v229, v229
	v_rcp_f32_e32 v230, v230
	v_rcp_f32_e32 v231, v231
	v_rcp_f32_e32 v232, v232
	v_rcp_f32_e32 v233, v233
	v_rcp_f32_e32 v234, v234
	v_rcp_f32_e32 v235, v235
	v_pk_mul_f32 v[120:121], v[128:129], v[120:121]
	v_pk_mul_f32 v[122:123], v[130:131], v[122:123]
	v_pk_mul_f32 v[116:117], v[124:125], v[116:117]
	v_pk_mul_f32 v[118:119], v[126:127], v[118:119]
	v_pk_mul_f32 v[128:129], v[120:121], v[228:229]
	v_pk_mul_f32 v[130:131], v[122:123], v[230:231]
	v_pk_mul_f32 v[124:125], v[116:117], v[232:233]
	v_pk_mul_f32 v[126:127], v[118:119], v[234:235]
	v_cvt_pk_bf16_f32 v128, v128, v129
	v_cvt_pk_bf16_f32 v129, v130, v131
	v_cvt_pk_bf16_f32 v130, v124, v125
	v_cvt_pk_bf16_f32 v131, v126, v127
	global_store_dwordx4 v252, v[128:131], s[4:5]
	v_pk_mul_f32 v[228:229], v[112:113], v[244:245] op_sel:[0,1] op_sel_hi:[1,1]
	v_pk_mul_f32 v[230:231], v[114:115], v[244:245] op_sel:[0,1] op_sel_hi:[1,1]
	v_pk_mul_f32 v[232:233], v[108:109], v[244:245] op_sel:[0,1] op_sel_hi:[1,1]
	v_pk_mul_f32 v[234:235], v[110:111], v[244:245] op_sel:[0,1] op_sel_hi:[1,1]
	v_exp_f32_e32 v228, v228
	v_exp_f32_e32 v229, v229
	v_exp_f32_e32 v230, v230
	v_exp_f32_e32 v231, v231
	v_exp_f32_e32 v232, v232
	v_exp_f32_e32 v233, v233
	v_exp_f32_e32 v234, v234
	v_exp_f32_e32 v235, v235
	v_pk_fma_f32 v[228:229], v[228:229], v[236:237], v[236:237] op_sel:[0,1,1] op_sel_hi:[1,1,1]
	v_pk_fma_f32 v[230:231], v[230:231], v[236:237], v[236:237] op_sel:[0,1,1] op_sel_hi:[1,1,1]
	v_pk_fma_f32 v[232:233], v[232:233], v[236:237], v[236:237] op_sel:[0,1,1] op_sel_hi:[1,1,1]
	v_pk_fma_f32 v[234:235], v[234:235], v[236:237], v[236:237] op_sel:[0,1,1] op_sel_hi:[1,1,1]
	v_rcp_f32_e32 v228, v228
	v_rcp_f32_e32 v229, v229
	v_rcp_f32_e32 v230, v230
	v_rcp_f32_e32 v231, v231
	v_rcp_f32_e32 v232, v232
	v_rcp_f32_e32 v233, v233
	v_rcp_f32_e32 v234, v234
	v_rcp_f32_e32 v235, v235
	v_pk_mul_f32 v[104:105], v[112:113], v[104:105]
	v_pk_mul_f32 v[106:107], v[114:115], v[106:107]
	v_pk_mul_f32 v[100:101], v[108:109], v[100:101]
	v_pk_mul_f32 v[102:103], v[110:111], v[102:103]
	v_add_u32_e32 v252, 0x16000, v252
	v_pk_mul_f32 v[112:113], v[104:105], v[228:229]
	v_pk_mul_f32 v[114:115], v[106:107], v[230:231]
	v_pk_mul_f32 v[108:109], v[100:101], v[232:233]
	v_pk_mul_f32 v[110:111], v[102:103], v[234:235]
	v_cvt_pk_bf16_f32 v104, v112, v113
	v_cvt_pk_bf16_f32 v105, v114, v115
	v_cvt_pk_bf16_f32 v106, v108, v109
	v_cvt_pk_bf16_f32 v107, v110, v111
	global_store_dwordx4 v252, v[104:107], s[4:5]
	v_pk_mul_f32 v[228:229], v[96:97], v[246:247] op_sel:[0,0] op_sel_hi:[1,0]
	v_pk_mul_f32 v[230:231], v[98:99], v[246:247] op_sel:[0,0] op_sel_hi:[1,0]
	v_pk_mul_f32 v[232:233], v[92:93], v[246:247] op_sel:[0,0] op_sel_hi:[1,0]
	v_pk_mul_f32 v[234:235], v[94:95], v[246:247] op_sel:[0,0] op_sel_hi:[1,0]
	v_exp_f32_e32 v228, v228
	v_exp_f32_e32 v229, v229
	v_exp_f32_e32 v230, v230
; __device__ __forceinline__ float sigm(float x) { return __builtin_amdgcn_rcpf(1.0f + __builtin_amdgcn_exp2f(-1.4426950408889634f * x)); }
; __device__ __forceinline__ u32x4 pack8(const f32x4 a, const f32x4 b) { u32x4 w; w.x = cvt_pk_bf16(a[0], a[1]); w.y = cvt_pk_bf16(a[2], a[3]); w.z = cvt_pk_bf16(b[0], b[1]); w.w = cvt_pk_bf16(b[2], b[3]); return w; }
;     __device__ __forceinline__ void operator()(const f32x4 (&acc)[2][2][4][2], const Unit& u, int wr, int wc, int fr, int fq) const {
;     ...
;             for (int m = 0; m < 4; ++m) { const float rf = rsr[ai * HALF + m * 16]; f32x4 v0 = acc[ai][0][m][0] * rf, v1 = acc[ai][0][m][1] * rf; const f32x4 u0 = acc[ai][1][m][0] * rf, u1 = acc[ai][1][m][1] * rf;
; #pragma unroll
;                 for (int e = 0; e < 4; ++e) { v0[e] = v0[e] * sigm(v0[e]) * u0[e]; v1[e] = v1[e] * sigm(v1[e]) * u1[e]; }
;                 *(u32x4*)(H + (size_t)(row0 + ai * HALF + m * 16) * DFF + col0) = pack8(v0, v1); } }
	v_exp_f32_e32 v231, v231
	v_exp_f32_e32 v232, v232
	v_exp_f32_e32 v233, v233
	v_exp_f32_e32 v234, v234
	v_exp_f32_e32 v235, v235
	v_pk_fma_f32 v[228:229], v[228:229], v[238:239], v[238:239] op_sel:[0,0,0] op_sel_hi:[1,0,0]
	v_pk_fma_f32 v[230:231], v[230:231], v[238:239], v[238:239] op_sel:[0,0,0] op_sel_hi:[1,0,0]
	v_pk_fma_f32 v[232:233], v[232:233], v[238:239], v[238:239] op_sel:[0,0,0] op_sel_hi:[1,0,0]
	v_pk_fma_f32 v[234:235], v[234:235], v[238:239], v[238:239] op_sel:[0,0,0] op_sel_hi:[1,0,0]
	v_rcp_f32_e32 v228, v228
	v_rcp_f32_e32 v229, v229
	v_rcp_f32_e32 v230, v230
	v_rcp_f32_e32 v231, v231
	v_rcp_f32_e32 v232, v232
	v_rcp_f32_e32 v233, v233
	v_rcp_f32_e32 v234, v234
	v_rcp_f32_e32 v235, v235
	v_pk_mul_f32 v[88:89], v[96:97], v[88:89]
	v_pk_mul_f32 v[90:91], v[98:99], v[90:91]
	v_pk_mul_f32 v[84:85], v[92:93], v[84:85]
	v_pk_mul_f32 v[86:87], v[94:95], v[86:87]
	v_add_u32_e32 v252, 0x16000, v252
	v_pk_mul_f32 v[96:97], v[88:89], v[228:229]
	v_pk_mul_f32 v[98:99], v[90:91], v[230:231]
	v_pk_mul_f32 v[92:93], v[84:85], v[232:233]
	v_pk_mul_f32 v[94:95], v[86:87], v[234:235]
	v_cvt_pk_bf16_f32 v96, v96, v97
	v_cvt_pk_bf16_f32 v97, v98, v99
	v_cvt_pk_bf16_f32 v98, v92, v93
	v_cvt_pk_bf16_f32 v99, v94, v95
	global_store_dwordx4 v252, v[96:99], s[4:5]
	v_pk_mul_f32 v[228:229], v[80:81], v[246:247] op_sel:[0,1] op_sel_hi:[1,1]
	v_pk_mul_f32 v[230:231], v[82:83], v[246:247] op_sel:[0,1] op_sel_hi:[1,1]
	v_pk_mul_f32 v[232:233], v[76:77], v[246:247] op_sel:[0,1] op_sel_hi:[1,1]
	v_pk_mul_f32 v[234:235], v[78:79], v[246:247] op_sel:[0,1] op_sel_hi:[1,1]
	v_exp_f32_e32 v228, v228
	v_exp_f32_e32 v229, v229
	v_exp_f32_e32 v230, v230
	v_exp_f32_e32 v231, v231
	v_exp_f32_e32 v232, v232
	v_exp_f32_e32 v233, v233
	v_exp_f32_e32 v234, v234
	v_exp_f32_e32 v235, v235
	v_pk_fma_f32 v[228:229], v[228:229], v[238:239], v[238:239] op_sel:[0,1,1] op_sel_hi:[1,1,1]
	v_pk_fma_f32 v[230:231], v[230:231], v[238:239], v[238:239] op_sel:[0,1,1] op_sel_hi:[1,1,1]
	v_pk_fma_f32 v[232:233], v[232:233], v[238:239], v[238:239] op_sel:[0,1,1] op_sel_hi:[1,1,1]
	v_pk_fma_f32 v[234:235], v[234:235], v[238:239], v[238:239] op_sel:[0,1,1] op_sel_hi:[1,1,1]
	v_rcp_f32_e32 v228, v228
	v_rcp_f32_e32 v229, v229
	v_rcp_f32_e32 v230, v230
	v_rcp_f32_e32 v231, v231
	v_rcp_f32_e32 v232, v232
	v_rcp_f32_e32 v233, v233
	v_rcp_f32_e32 v234, v234
	v_rcp_f32_e32 v235, v235
	v_pk_mul_f32 v[72:73], v[80:81], v[72:73]
	v_pk_mul_f32 v[74:75], v[82:83], v[74:75]
	v_pk_mul_f32 v[68:69], v[76:77], v[68:69]
	v_pk_mul_f32 v[70:71], v[78:79], v[70:71]
	v_add_u32_e32 v252, 0x16000, v252
	v_pk_mul_f32 v[80:81], v[72:73], v[228:229]
	v_pk_mul_f32 v[82:83], v[74:75], v[230:231]
	v_pk_mul_f32 v[76:77], v[68:69], v[232:233]
	v_pk_mul_f32 v[78:79], v[70:71], v[234:235]
	v_cvt_pk_bf16_f32 v72, v80, v81
	v_cvt_pk_bf16_f32 v73, v82, v83
	v_cvt_pk_bf16_f32 v74, v76, v77
	v_cvt_pk_bf16_f32 v75, v78, v79
	global_store_dwordx4 v252, v[72:75], s[4:5]
	v_pk_mul_f32 v[228:229], v[64:65], v[248:249] op_sel:[0,0] op_sel_hi:[1,0]
	v_pk_mul_f32 v[230:231], v[66:67], v[248:249] op_sel:[0,0] op_sel_hi:[1,0]
	v_pk_mul_f32 v[232:233], v[60:61], v[248:249] op_sel:[0,0] op_sel_hi:[1,0]
	v_pk_mul_f32 v[234:235], v[62:63], v[248:249] op_sel:[0,0] op_sel_hi:[1,0]
	v_exp_f32_e32 v228, v228
	v_exp_f32_e32 v229, v229
	v_exp_f32_e32 v230, v230
	v_exp_f32_e32 v231, v231
	v_exp_f32_e32 v232, v232
	v_exp_f32_e32 v233, v233
	v_exp_f32_e32 v234, v234
	v_exp_f32_e32 v235, v235
	v_pk_fma_f32 v[228:229], v[228:229], v[240:241], v[240:241] op_sel:[0,0,0] op_sel_hi:[1,0,0]
	v_pk_fma_f32 v[230:231], v[230:231], v[240:241], v[240:241] op_sel:[0,0,0] op_sel_hi:[1,0,0]
	v_pk_fma_f32 v[232:233], v[232:233], v[240:241], v[240:241] op_sel:[0,0,0] op_sel_hi:[1,0,0]
	v_pk_fma_f32 v[234:235], v[234:235], v[240:241], v[240:241] op_sel:[0,0,0] op_sel_hi:[1,0,0]
	v_rcp_f32_e32 v228, v228
	v_rcp_f32_e32 v229, v229
	v_rcp_f32_e32 v230, v230
	v_rcp_f32_e32 v231, v231
	v_rcp_f32_e32 v232, v232
	v_rcp_f32_e32 v233, v233
	v_rcp_f32_e32 v234, v234
	v_rcp_f32_e32 v235, v235
	v_pk_mul_f32 v[56:57], v[64:65], v[56:57]
	v_pk_mul_f32 v[58:59], v[66:67], v[58:59]
	v_pk_mul_f32 v[52:53], v[60:61], v[52:53]
	v_pk_mul_f32 v[54:55], v[62:63], v[54:55]
	v_add_u32_e32 v252, 0x6e000, v252
	v_pk_mul_f32 v[64:65], v[56:57], v[228:229]
	v_pk_mul_f32 v[66:67], v[58:59], v[230:231]
	v_pk_mul_f32 v[60:61], v[52:53], v[232:233]
	v_pk_mul_f32 v[62:63], v[54:55], v[234:235]
	v_cvt_pk_bf16_f32 v64, v64, v65
	v_cvt_pk_bf16_f32 v65, v66, v67
	v_cvt_pk_bf16_f32 v66, v60, v61
	v_cvt_pk_bf16_f32 v67, v62, v63
	global_store_dwordx4 v252, v[64:67], s[4:5]
	v_pk_mul_f32 v[228:229], v[48:49], v[248:249] op_sel:[0,1] op_sel_hi:[1,1]
	v_pk_mul_f32 v[230:231], v[50:51], v[248:249] op_sel:[0,1] op_sel_hi:[1,1]
	v_pk_mul_f32 v[232:233], v[44:45], v[248:249] op_sel:[0,1] op_sel_hi:[1,1]
	v_pk_mul_f32 v[234:235], v[46:47], v[248:249] op_sel:[0,1] op_sel_hi:[1,1]
; __device__ __forceinline__ float sigm(float x) { return __builtin_amdgcn_rcpf(1.0f + __builtin_amdgcn_exp2f(-1.4426950408889634f * x)); }
; __device__ __forceinline__ u32x4 pack8(const f32x4 a, const f32x4 b) { u32x4 w; w.x = cvt_pk_bf16(a[0], a[1]); w.y = cvt_pk_bf16(a[2], a[3]); w.z = cvt_pk_bf16(b[0], b[1]); w.w = cvt_pk_bf16(b[2], b[3]); return w; }
;     __device__ __forceinline__ void operator()(const f32x4 (&acc)[2][2][4][2], const Unit& u, int wr, int wc, int fr, int fq) const {
;     ...
;             for (int m = 0; m < 4; ++m) { const float rf = rsr[ai * HALF + m * 16]; f32x4 v0 = acc[ai][0][m][0] * rf, v1 = acc[ai][0][m][1] * rf; const f32x4 u0 = acc[ai][1][m][0] * rf, u1 = acc[ai][1][m][1] * rf;
; #pragma unroll
;                 for (int e = 0; e < 4; ++e) { v0[e] = v0[e] * sigm(v0[e]) * u0[e]; v1[e] = v1[e] * sigm(v1[e]) * u1[e]; }
;                 *(u32x4*)(H + (size_t)(row0 + ai * HALF + m * 16) * DFF + col0) = pack8(v0, v1); } }
	v_exp_f32_e32 v228, v228
	v_exp_f32_e32 v229, v229
	v_exp_f32_e32 v230, v230
	v_exp_f32_e32 v231, v231
	v_exp_f32_e32 v232, v232
	v_exp_f32_e32 v233, v233
	v_exp_f32_e32 v234, v234
	v_exp_f32_e32 v235, v235
	v_pk_fma_f32 v[228:229], v[228:229], v[240:241], v[240:241] op_sel:[0,1,1] op_sel_hi:[1,1,1]
	v_pk_fma_f32 v[230:231], v[230:231], v[240:241], v[240:241] op_sel:[0,1,1] op_sel_hi:[1,1,1]
	v_pk_fma_f32 v[232:233], v[232:233], v[240:241], v[240:241] op_sel:[0,1,1] op_sel_hi:[1,1,1]
	v_pk_fma_f32 v[234:235], v[234:235], v[240:241], v[240:241] op_sel:[0,1,1] op_sel_hi:[1,1,1]
	v_rcp_f32_e32 v228, v228
	v_rcp_f32_e32 v229, v229
	v_rcp_f32_e32 v230, v230
	v_rcp_f32_e32 v231, v231
	v_rcp_f32_e32 v232, v232
	v_rcp_f32_e32 v233, v233
	v_rcp_f32_e32 v234, v234
	v_rcp_f32_e32 v235, v235
	v_pk_mul_f32 v[40:41], v[48:49], v[40:41]
	v_pk_mul_f32 v[42:43], v[50:51], v[42:43]
	v_pk_mul_f32 v[36:37], v[44:45], v[36:37]
	v_pk_mul_f32 v[38:39], v[46:47], v[38:39]
	v_add_u32_e32 v252, 0x16000, v252
	v_pk_mul_f32 v[48:49], v[40:41], v[228:229]
	v_pk_mul_f32 v[50:51], v[42:43], v[230:231]
	v_pk_mul_f32 v[44:45], v[36:37], v[232:233]
	v_pk_mul_f32 v[46:47], v[38:39], v[234:235]
	v_cvt_pk_bf16_f32 v40, v48, v49
	v_cvt_pk_bf16_f32 v41, v50, v51
	v_cvt_pk_bf16_f32 v42, v44, v45
	v_cvt_pk_bf16_f32 v43, v46, v47
	global_store_dwordx4 v252, v[40:43], s[4:5]
	v_pk_mul_f32 v[228:229], v[32:33], v[250:251] op_sel:[0,0] op_sel_hi:[1,0]
	v_pk_mul_f32 v[230:231], v[34:35], v[250:251] op_sel:[0,0] op_sel_hi:[1,0]
	v_pk_mul_f32 v[232:233], v[28:29], v[250:251] op_sel:[0,0] op_sel_hi:[1,0]
	v_pk_mul_f32 v[234:235], v[30:31], v[250:251] op_sel:[0,0] op_sel_hi:[1,0]
	v_exp_f32_e32 v228, v228
	v_exp_f32_e32 v229, v229
	v_exp_f32_e32 v230, v230
	v_exp_f32_e32 v231, v231
	v_exp_f32_e32 v232, v232
	v_exp_f32_e32 v233, v233
	v_exp_f32_e32 v234, v234
	v_exp_f32_e32 v235, v235
	v_pk_fma_f32 v[228:229], v[228:229], v[242:243], v[242:243] op_sel:[0,0,0] op_sel_hi:[1,0,0]
	v_pk_fma_f32 v[230:231], v[230:231], v[242:243], v[242:243] op_sel:[0,0,0] op_sel_hi:[1,0,0]
	v_pk_fma_f32 v[232:233], v[232:233], v[242:243], v[242:243] op_sel:[0,0,0] op_sel_hi:[1,0,0]
	v_pk_fma_f32 v[234:235], v[234:235], v[242:243], v[242:243] op_sel:[0,0,0] op_sel_hi:[1,0,0]
	v_rcp_f32_e32 v228, v228
	v_rcp_f32_e32 v229, v229
	v_rcp_f32_e32 v230, v230
	v_rcp_f32_e32 v231, v231
	v_rcp_f32_e32 v232, v232
	v_rcp_f32_e32 v233, v233
	v_rcp_f32_e32 v234, v234
	v_rcp_f32_e32 v235, v235
	v_pk_mul_f32 v[24:25], v[32:33], v[24:25]
	v_pk_mul_f32 v[26:27], v[34:35], v[26:27]
	v_pk_mul_f32 v[20:21], v[28:29], v[20:21]
	v_pk_mul_f32 v[22:23], v[30:31], v[22:23]
	v_add_u32_e32 v252, 0x16000, v252
	v_pk_mul_f32 v[32:33], v[24:25], v[228:229]
	v_pk_mul_f32 v[34:35], v[26:27], v[230:231]
	v_pk_mul_f32 v[28:29], v[20:21], v[232:233]
	v_pk_mul_f32 v[30:31], v[22:23], v[234:235]
	v_cvt_pk_bf16_f32 v32, v32, v33
	v_cvt_pk_bf16_f32 v33, v34, v35
	v_cvt_pk_bf16_f32 v34, v28, v29
	v_cvt_pk_bf16_f32 v35, v30, v31
	global_store_dwordx4 v252, v[32:35], s[4:5]
	v_pk_mul_f32 v[228:229], v[16:17], v[250:251] op_sel:[0,1] op_sel_hi:[1,1]
	v_pk_mul_f32 v[230:231], v[18:19], v[250:251] op_sel:[0,1] op_sel_hi:[1,1]
	v_pk_mul_f32 v[232:233], v[12:13], v[250:251] op_sel:[0,1] op_sel_hi:[1,1]
	v_pk_mul_f32 v[234:235], v[14:15], v[250:251] op_sel:[0,1] op_sel_hi:[1,1]
	v_exp_f32_e32 v228, v228
	v_exp_f32_e32 v229, v229
	v_exp_f32_e32 v230, v230
	v_exp_f32_e32 v231, v231
	v_exp_f32_e32 v232, v232
	v_exp_f32_e32 v233, v233
	v_exp_f32_e32 v234, v234
	v_exp_f32_e32 v235, v235
	v_pk_fma_f32 v[228:229], v[228:229], v[242:243], v[242:243] op_sel:[0,1,1] op_sel_hi:[1,1,1]
	v_pk_fma_f32 v[230:231], v[230:231], v[242:243], v[242:243] op_sel:[0,1,1] op_sel_hi:[1,1,1]
	v_pk_fma_f32 v[232:233], v[232:233], v[242:243], v[242:243] op_sel:[0,1,1] op_sel_hi:[1,1,1]
	v_pk_fma_f32 v[234:235], v[234:235], v[242:243], v[242:243] op_sel:[0,1,1] op_sel_hi:[1,1,1]
	v_rcp_f32_e32 v228, v228
	v_rcp_f32_e32 v229, v229
	v_rcp_f32_e32 v230, v230
	v_rcp_f32_e32 v231, v231
	v_rcp_f32_e32 v232, v232
	v_rcp_f32_e32 v233, v233
	v_rcp_f32_e32 v234, v234
	v_rcp_f32_e32 v235, v235
	v_pk_mul_f32 v[8:9], v[16:17], v[8:9]
	v_pk_mul_f32 v[10:11], v[18:19], v[10:11]
	v_pk_mul_f32 v[4:5], v[12:13], v[4:5]
	v_pk_mul_f32 v[6:7], v[14:15], v[6:7]
	v_add_u32_e32 v252, 0x16000, v252
	v_pk_mul_f32 v[16:17], v[8:9], v[228:229]
	v_pk_mul_f32 v[18:19], v[10:11], v[230:231]
	v_pk_mul_f32 v[12:13], v[4:5], v[232:233]
	v_pk_mul_f32 v[14:15], v[6:7], v[234:235]
	v_cvt_pk_bf16_f32 v8, v16, v17
	v_cvt_pk_bf16_f32 v9, v18, v19
	v_cvt_pk_bf16_f32 v10, v12, v13
	v_cvt_pk_bf16_f32 v11, v14, v15
	global_store_dwordx4 v252, v[8:11], s[4:5]
	s_andn2_b64 vcc, exec, s[38:39]
	s_mov_b64 s[0:1], -1
	s_cbranch_vccnz .LBB0_1473
	s_andn2_b64 vcc, exec, s[8:9]
	s_cbranch_vccnz .LBB0_1472
	s_barrier
	s_branch .LBB0_1472
